# main: Wv fragment loads spread through the exp/sum and y phases instead of the scores phase
# baseline (speedup 1.0000x reference)
_Z7na_mainPKDF16_PKhS0_PKfS4_S4_S4_Pf:
	s_lshl_b32 s3, s2, 5
	s_and_b32 s3, s3, 0xe0
	s_ashr_i32 s2, s2, 3
	s_add_i32 s3, s3, s2
	s_ashr_i32 s2, s3, 6
	s_lshl_b32 s3, s3, 5
	s_and_b32 s14, s3, 0x7e0
	v_mov_b32_e32 v1, 0x7c0
	s_load_dwordx8 s[4:11], s[0:1], 0x0
	s_load_dwordx2 s[18:19], s[0:1], 0x20
	v_med3_u32 v1, s14, 32, v1
	v_subrev_u32_e32 v97, 32, v1
	s_ashr_i32 s3, s2, 31
	v_lshlrev_b32_e32 v58, 1, v97
	s_lshl_b64 s[12:13], s[2:3], 12
	v_mov_b32_e32 v59, 0
	v_sub_u32_e32 v60, s14, v97
	v_lshl_add_u64 v[10:11], s[12:13], 0, v[58:59]
	v_lshlrev_b64 v[2:3], 9, v[10:11]
	v_lshl_or_b32 v22, v60, 6, v0
	s_waitcnt lgkmcnt(0)
	s_mov_b32 s20, s8
	s_mov_b32 s21, s9
	v_and_b32_e32 v208, 31, v0
	v_lshlrev_b32_e32 v208, 5, v208
	global_load_dwordx4 v[192:195], v208, s[18:19]
	global_load_dwordx4 v[196:199], v208, s[18:19] offset:16
	v_lshl_add_u64 v[20:21], s[4:5], 0, v[2:3]
	v_ashrrev_i32_e32 v23, 31, v22
	v_lshl_add_u64 v[2:3], v[22:23], 4, v[20:21]
	global_load_dwordx4 v[12:15], v[2:3], off
	v_or_b32_e32 v28, 0x200, v22
	v_ashrrev_i32_e32 v29, 31, v28
	v_lshl_add_u64 v[2:3], v[28:29], 4, v[20:21]
	global_load_dwordx4 v[16:19], v[2:3], off
	v_or_b32_e32 v184, 0x400, v22
	v_ashrrev_i32_e32 v185, 31, v184
	v_lshl_add_u64 v[184:185], v[184:185], 4, v[20:21]
	v_or_b32_e32 v188, 0x600, v22
	v_ashrrev_i32_e32 v189, 31, v188
	v_lshl_add_u64 v[188:189], v[188:189], 4, v[20:21]
	global_load_dwordx4 v[184:187], v[184:185], off
	global_load_dwordx4 v[188:191], v[188:189], off
	v_lshrrev_b32_e32 v99, 6, v0
	v_and_b32_e32 v98, 63, v0
	v_lshlrev_b32_e32 v118, 13, v99
	v_lshl_or_b32 v58, v98, 5, v118
	s_movk_i32 s15, 0x1000
	v_lshl_add_u64 v[24:25], s[6:7], 0, v[58:59]
	v_or_b32_e32 v32, 0x400, v22
	v_or_b32_e32 v62, 0x600, v22
	v_add_co_u32_e32 v64, vcc, s15, v24
	s_mov_b64 s[12:13], 0x1000
	s_mov_b64 s[16:17], 0x1800
	v_lshlrev_b32_e32 v72, 1, v60
	v_lshrrev_b32_e32 v23, 5, v22
	v_and_b32_e32 v34, 32, v22
	v_ashrrev_i32_e32 v33, 31, v32
	v_ashrrev_i32_e32 v63, 31, v62
	v_addc_co_u32_e32 v65, vcc, 0, v25, vcc
	global_load_dwordx4 v[6:9], v58, s[6:7] offset:16
	global_load_dwordx4 v[2:5], v58, s[6:7]
	global_load_dwordx4 v[54:57], v58, s[6:7] offset:2064
	global_load_dwordx4 v[50:53], v58, s[6:7] offset:2048
	v_lshrrev_b32_e32 v58, 6, v22
	v_bfe_u32 v73, v22, 8, 2
	v_lshl_add_u64 v[26:27], v[24:25], 0, s[12:13]
	v_lshl_add_u64 v[24:25], v[24:25], 0, s[16:17]
	v_cmp_ne_u32_e32 vcc, 0, v34
	v_sub_u32_e32 v75, v23, v72
	global_load_dwordx4 v[42:45], v[64:65], off
	global_load_dwordx4 v[46:49], v[26:27], off offset:16
	global_load_dwordx4 v[34:37], v[64:65], off offset:2048
	global_load_dwordx4 v[38:41], v[24:25], off offset:16
	v_mov_b32_e32 v61, 0x60
	v_cndmask_b32_e32 v74, 0, v61, vcc
	v_add_u32_e32 v33, v74, v58
	v_lshlrev_b32_e32 v64, 2, v33
	v_bfe_u32 v96, v0, 4, 1
	v_and_b32_e32 v100, 15, v0
	v_mov_b32_e32 v30, v59
	v_mov_b32_e32 v31, v59
	v_and_b32_e32 v64, 12, v64
	v_mul_u32_u24_e32 v29, 0xc000, v96
	v_bitop3_b32 v64, v64, v100, v73 bitop3:0x36
	v_lshl_or_b32 v64, v64, 4, v29
	v_lshlrev_b32_e32 v63, 1, v75
	v_lshl_add_u32 v33, v33, 8, v64
	v_bfe_u32 v71, v0, 1, 4
	v_and_b32_e32 v70, 32, v0
	v_lshlrev_b32_e32 v1, 3, v0
	v_lshrrev_b32_e32 v58, 1, v75
	v_and_b32_e32 v1, 8, v1
	v_add_lshl_u32 v58, v58, v70, 8
	v_lshlrev_b32_e32 v121, 3, v99
	v_bfe_u32 v101, v0, 4, 2
	v_lshlrev_b32_e32 v102, 2, v101
	v_and_b32_e32 v116, 31, v0
	v_bfe_u32 v119, v0, 5, 1
	v_lshlrev_b32_e32 v124, 1, v119
	v_lshlrev_b32_e32 v117, 8, v116
	v_lshrrev_b32_e32 v95, 4, v0
	s_movk_i32 s16, 0x60
	s_mov_b32 s17, 0xc000
	v_and_b32_e32 v211, 3, v99
	v_lshrrev_b32_e32 v212, 2, v99
	v_lshl_or_b32 v211, v211, 2, v212
	v_xor_b32_e32 v213, v100, v211
	v_mul_u32_u24_e32 v214, 0x60, v119
	v_add3_u32 v214, v214, v60, v99
	v_mul_u32_u24_e32 v215, 0xc000, v96
	v_lshl_add_u32 v214, v214, 8, v215
	v_lshl_or_b32 v220, v213, 4, v214
	v_xor_b32_e32 v221, 32, v220
	v_xor_b32_e32 v216, v71, v211
	v_lshl_add_u32 v217, v119, 5, v99
	v_lshlrev_b32_e32 v217, 8, v217
	v_lshl_or_b32 v216, v216, 4, v217
	v_or_b32_e32 v216, v216, v1
	v_add_u32_e32 v222, 0x23800, v216
	v_xor_b32_e32 v223, 32, v222
	s_waitcnt vmcnt(11)
	ds_write_b128 v220, v[12:15]
	v_fma_mix_f32 v200, v192, v12, 0 op_sel_hi:[0,1,0]
	v_fma_mix_f32 v201, v193, v12, 0 op_sel:[0,1,0] op_sel_hi:[0,1,0]
	v_cvt_f32_f16_e32 v211, v12
	v_cvt_f32_f16_sdwa v212, v12 dst_sel:DWORD dst_unused:UNUSED_PAD src0_sel:WORD_1
	v_fma_mix_f32 v200, v194, v13, v200 op_sel_hi:[0,1,0]
	v_fma_mix_f32 v201, v195, v13, v201 op_sel:[0,1,0] op_sel_hi:[0,1,0]
	v_cvt_f32_f16_e32 v213, v13
	v_cvt_f32_f16_sdwa v214, v13 dst_sel:DWORD dst_unused:UNUSED_PAD src0_sel:WORD_1
	v_fma_mix_f32 v200, v196, v14, v200 op_sel_hi:[0,1,0]
	v_fma_mix_f32 v201, v197, v14, v201 op_sel:[0,1,0] op_sel_hi:[0,1,0]
	v_cvt_f32_f16_e32 v215, v14
	v_cvt_f32_f16_sdwa v216, v14 dst_sel:DWORD dst_unused:UNUSED_PAD src0_sel:WORD_1
	v_fma_mix_f32 v200, v198, v15, v200 op_sel_hi:[0,1,0]
	v_fma_mix_f32 v201, v199, v15, v201 op_sel:[0,1,0] op_sel_hi:[0,1,0]
	v_cvt_f32_f16_e32 v217, v15
	v_cvt_f32_f16_sdwa v218, v15 dst_sel:DWORD dst_unused:UNUSED_PAD src0_sel:WORD_1
	v_cvt_pk_fp8_f32 v224, v211, v212
	v_cvt_pk_fp8_f32 v225, v215, v216
	v_cvt_pk_fp8_f32 v224, v213, v214 op_sel:[0,0,1]
	v_cvt_pk_fp8_f32 v225, v217, v218 op_sel:[0,0,1]
	s_nop 0
	ds_write_b64 v222, v[224:225]
	s_waitcnt vmcnt(10)
	ds_write_b128 v221, v[16:19] offset:2048
	v_fma_mix_f32 v202, v192, v16, 0 op_sel_hi:[0,1,0]
	v_fma_mix_f32 v203, v193, v16, 0 op_sel:[0,1,0] op_sel_hi:[0,1,0]
	v_cvt_f32_f16_e32 v211, v16
	v_cvt_f32_f16_sdwa v212, v16 dst_sel:DWORD dst_unused:UNUSED_PAD src0_sel:WORD_1
	v_fma_mix_f32 v202, v194, v17, v202 op_sel_hi:[0,1,0]
	v_fma_mix_f32 v203, v195, v17, v203 op_sel:[0,1,0] op_sel_hi:[0,1,0]
	v_cvt_f32_f16_e32 v213, v17
	v_cvt_f32_f16_sdwa v214, v17 dst_sel:DWORD dst_unused:UNUSED_PAD src0_sel:WORD_1
	v_fma_mix_f32 v202, v196, v18, v202 op_sel_hi:[0,1,0]
	v_fma_mix_f32 v203, v197, v18, v203 op_sel:[0,1,0] op_sel_hi:[0,1,0]
	v_cvt_f32_f16_e32 v215, v18
	v_cvt_f32_f16_sdwa v216, v18 dst_sel:DWORD dst_unused:UNUSED_PAD src0_sel:WORD_1
	v_fma_mix_f32 v202, v198, v19, v202 op_sel_hi:[0,1,0]
	v_fma_mix_f32 v203, v199, v19, v203 op_sel:[0,1,0] op_sel_hi:[0,1,0]
	v_cvt_f32_f16_e32 v217, v19
	v_cvt_f32_f16_sdwa v218, v19 dst_sel:DWORD dst_unused:UNUSED_PAD src0_sel:WORD_1
	v_cvt_pk_fp8_f32 v226, v211, v212
	v_cvt_pk_fp8_f32 v227, v215, v216
	v_cvt_pk_fp8_f32 v226, v213, v214 op_sel:[0,0,1]
	v_cvt_pk_fp8_f32 v227, v217, v218 op_sel:[0,0,1]
	s_nop 0
	ds_write_b64 v223, v[226:227] offset:2048
	s_waitcnt vmcnt(9)
	ds_write_b128 v220, v[184:187] offset:4096
	v_fma_mix_f32 v204, v192, v184, 0 op_sel_hi:[0,1,0]
	v_fma_mix_f32 v205, v193, v184, 0 op_sel:[0,1,0] op_sel_hi:[0,1,0]
	v_cvt_f32_f16_e32 v211, v184
	v_cvt_f32_f16_sdwa v212, v184 dst_sel:DWORD dst_unused:UNUSED_PAD src0_sel:WORD_1
	v_fma_mix_f32 v204, v194, v185, v204 op_sel_hi:[0,1,0]
	v_fma_mix_f32 v205, v195, v185, v205 op_sel:[0,1,0] op_sel_hi:[0,1,0]
	v_cvt_f32_f16_e32 v213, v185
	v_cvt_f32_f16_sdwa v214, v185 dst_sel:DWORD dst_unused:UNUSED_PAD src0_sel:WORD_1
	v_fma_mix_f32 v204, v196, v186, v204 op_sel_hi:[0,1,0]
	v_fma_mix_f32 v205, v197, v186, v205 op_sel:[0,1,0] op_sel_hi:[0,1,0]
	v_cvt_f32_f16_e32 v215, v186
	v_cvt_f32_f16_sdwa v216, v186 dst_sel:DWORD dst_unused:UNUSED_PAD src0_sel:WORD_1
	v_fma_mix_f32 v204, v198, v187, v204 op_sel_hi:[0,1,0]
	v_fma_mix_f32 v205, v199, v187, v205 op_sel:[0,1,0] op_sel_hi:[0,1,0]
	v_cvt_f32_f16_e32 v217, v187
	v_cvt_f32_f16_sdwa v218, v187 dst_sel:DWORD dst_unused:UNUSED_PAD src0_sel:WORD_1
	v_cvt_pk_fp8_f32 v228, v211, v212
	v_cvt_pk_fp8_f32 v229, v215, v216
	v_cvt_pk_fp8_f32 v228, v213, v214 op_sel:[0,0,1]
	v_cvt_pk_fp8_f32 v229, v217, v218 op_sel:[0,0,1]
	s_nop 0
	ds_write_b64 v222, v[228:229] offset:4096
	s_waitcnt vmcnt(8)
	ds_write_b128 v221, v[188:191] offset:6144
	v_fma_mix_f32 v206, v192, v188, 0 op_sel_hi:[0,1,0]
	v_fma_mix_f32 v207, v193, v188, 0 op_sel:[0,1,0] op_sel_hi:[0,1,0]
	v_cvt_f32_f16_e32 v211, v188
	v_cvt_f32_f16_sdwa v212, v188 dst_sel:DWORD dst_unused:UNUSED_PAD src0_sel:WORD_1
	v_fma_mix_f32 v206, v194, v189, v206 op_sel_hi:[0,1,0]
	v_fma_mix_f32 v207, v195, v189, v207 op_sel:[0,1,0] op_sel_hi:[0,1,0]
	v_cvt_f32_f16_e32 v213, v189
	v_cvt_f32_f16_sdwa v214, v189 dst_sel:DWORD dst_unused:UNUSED_PAD src0_sel:WORD_1
	v_fma_mix_f32 v206, v196, v190, v206 op_sel_hi:[0,1,0]
	v_fma_mix_f32 v207, v197, v190, v207 op_sel:[0,1,0] op_sel_hi:[0,1,0]
	v_cvt_f32_f16_e32 v215, v190
	v_cvt_f32_f16_sdwa v216, v190 dst_sel:DWORD dst_unused:UNUSED_PAD src0_sel:WORD_1
	v_fma_mix_f32 v206, v198, v191, v206 op_sel_hi:[0,1,0]
	v_fma_mix_f32 v207, v199, v191, v207 op_sel:[0,1,0] op_sel_hi:[0,1,0]
	v_cvt_f32_f16_e32 v217, v191
	v_cvt_f32_f16_sdwa v218, v191 dst_sel:DWORD dst_unused:UNUSED_PAD src0_sel:WORD_1
	v_cvt_pk_fp8_f32 v230, v211, v212
	v_cvt_pk_fp8_f32 v231, v215, v216
	v_cvt_pk_fp8_f32 v230, v213, v214 op_sel:[0,0,1]
	v_cvt_pk_fp8_f32 v231, v217, v218 op_sel:[0,0,1]
	s_nop 0
	ds_write_b64 v223, v[230:231] offset:6144
	v_add_f32_e32 v200, v200, v201
	v_add_f32_e32 v202, v202, v203
	v_add_f32_e32 v204, v204, v205
	v_add_f32_e32 v206, v206, v207
	v_lshlrev_b32_e32 v208, 7, v119
	v_lshl_add_u32 v208, v99, 2, v208
	v_add_u32_e32 v208, 0x27800, v208
	v_add_f32_dpp v200, v200, v200 quad_perm:[1,0,3,2] row_mask:0xf bank_mask:0xf
	v_add_f32_dpp v202, v202, v202 quad_perm:[1,0,3,2] row_mask:0xf bank_mask:0xf
	v_add_f32_dpp v204, v204, v204 quad_perm:[1,0,3,2] row_mask:0xf bank_mask:0xf
	v_add_f32_dpp v206, v206, v206 quad_perm:[1,0,3,2] row_mask:0xf bank_mask:0xf
	v_add_f32_dpp v200, v200, v200 quad_perm:[2,3,0,1] row_mask:0xf bank_mask:0xf
	v_add_f32_dpp v202, v202, v202 quad_perm:[2,3,0,1] row_mask:0xf bank_mask:0xf
	v_add_f32_dpp v204, v204, v204 quad_perm:[2,3,0,1] row_mask:0xf bank_mask:0xf
	v_add_f32_dpp v206, v206, v206 quad_perm:[2,3,0,1] row_mask:0xf bank_mask:0xf
	v_add_f32_dpp v200, v200, v200 row_half_mirror row_mask:0xf bank_mask:0xf
	v_add_f32_dpp v202, v202, v202 row_half_mirror row_mask:0xf bank_mask:0xf
	v_add_f32_dpp v204, v204, v204 row_half_mirror row_mask:0xf bank_mask:0xf
	v_add_f32_dpp v206, v206, v206 row_half_mirror row_mask:0xf bank_mask:0xf
	v_add_f32_dpp v200, v200, v200 row_mirror row_mask:0xf bank_mask:0xf
	v_add_f32_dpp v202, v202, v202 row_mirror row_mask:0xf bank_mask:0xf
	v_add_f32_dpp v204, v204, v204 row_mirror row_mask:0xf bank_mask:0xf
	v_add_f32_dpp v206, v206, v206 row_mirror row_mask:0xf bank_mask:0xf
	v_add_f32_dpp v200, v200, v200 row_bcast:15 row_mask:0xa bank_mask:0xf
	v_add_f32_dpp v202, v202, v202 row_bcast:15 row_mask:0xa bank_mask:0xf
	v_add_f32_dpp v204, v204, v204 row_bcast:15 row_mask:0xa bank_mask:0xf
	v_add_f32_dpp v206, v206, v206 row_bcast:15 row_mask:0xa bank_mask:0xf
	s_mov_b32 exec_lo, 0xffff0000
	s_mov_b32 exec_hi, 0xffff0000
	ds_write_b32 v208, v200
	ds_write_b32 v208, v202 offset:32
	ds_write_b32 v208, v204 offset:64
	ds_write_b32 v208, v206 offset:96
	s_mov_b64 exec, -1
	v_cmp_lt_i32_e32 vcc, v121, v60
	s_nop 0
	v_mov_b32_e32 v15, v59
	v_cndmask_b32_e64 v12, 32, 0, vcc
	v_add_u32_e32 v16, v12, v121
	v_or_b32_e32 v12, v16, v101
	v_lshlrev_b32_e32 v58, 1, v12
	v_lshrrev_b32_e32 v12, 5, v0
	v_and_b32_e32 v12, 2, v12
	v_bitop3_b32 v14, v102, v100, v12 bitop3:0x36
	v_lshl_add_u64 v[12:13], v[10:11], 0, v[58:59]
	v_lshlrev_b64 v[12:13], 9, v[12:13]
	v_lshlrev_b32_e32 v16, 8, v16
	v_lshl_add_u64 v[12:13], s[4:5], 0, v[12:13]
	v_lshlrev_b32_e32 v14, 4, v14
	v_readfirstlane_b32 s6, v16
	v_add_u32_e32 v17, 0xc000, v16
	v_lshl_add_u64 v[12:13], v[12:13], 0, v[14:15]
	s_mov_b32 m0, s6
	s_mov_b64 s[6:7], 0x100
	v_readfirstlane_b32 s12, v17
	global_load_lds_dwordx4 v[12:13], off
	v_lshl_add_u64 v[12:13], v[12:13], 0, s[6:7]
	s_mov_b32 m0, s12
	v_or_b32_e32 v58, 1, v58
	global_load_lds_dwordx4 v[12:13], off
	v_lshl_add_u64 v[12:13], v[10:11], 0, v[58:59]
	v_lshlrev_b64 v[12:13], 9, v[12:13]
	v_lshl_add_u64 v[12:13], s[4:5], 0, v[12:13]
	v_lshl_add_u64 v[12:13], v[12:13], 0, v[14:15]
	v_add_u32_e32 v14, 0x6000, v16
	v_bfe_u32 v61, v0, 2, 2
	v_readfirstlane_b32 s12, v14
	v_add_u32_e32 v14, 0x12000, v16
	s_mov_b32 m0, s12
	v_readfirstlane_b32 s12, v14
	global_load_lds_dwordx4 v[12:13], off
	v_lshl_add_u64 v[12:13], v[12:13], 0, s[6:7]
	s_mov_b32 m0, s12
	v_add_u32_e32 v18, 0x23800, v117
	global_load_lds_dwordx4 v[12:13], off
	v_or_b32_e32 v12, 4, v121
	v_cmp_lt_i32_e32 vcc, v12, v60
	s_nop 1
	v_cndmask_b32_e64 v13, 32, 0, vcc
	v_add_u32_e32 v16, v13, v12
	v_or_b32_e32 v13, v16, v101
	v_lshlrev_b32_e32 v58, 1, v13
	v_bfe_u32 v12, v12, 2, 2
	v_bitop3_b32 v14, v102, v100, v12 bitop3:0x36
	v_lshl_add_u64 v[12:13], v[10:11], 0, v[58:59]
	v_lshlrev_b64 v[12:13], 9, v[12:13]
	v_lshlrev_b32_e32 v16, 8, v16
	v_lshl_add_u64 v[12:13], s[4:5], 0, v[12:13]
	v_lshlrev_b32_e32 v14, 4, v14
	v_readfirstlane_b32 s12, v16
	v_add_u32_e32 v17, 0xc000, v16
	v_lshl_add_u64 v[12:13], v[12:13], 0, v[14:15]
	s_mov_b32 m0, s12
	v_readfirstlane_b32 s12, v17
	v_or_b32_e32 v58, 1, v58
	global_load_lds_dwordx4 v[12:13], off
	v_lshl_add_u64 v[12:13], v[12:13], 0, s[6:7]
	s_mov_b32 m0, s12
	v_lshl_add_u64 v[10:11], v[10:11], 0, v[58:59]
	global_load_lds_dwordx4 v[12:13], off
	v_lshlrev_b64 v[10:11], 9, v[10:11]
	v_add_u32_e32 v12, 0x6000, v16
	v_lshl_add_u64 v[10:11], s[4:5], 0, v[10:11]
	v_readfirstlane_b32 s4, v12
	v_add_u32_e32 v12, 0x12000, v16
	v_lshl_add_u64 v[10:11], v[10:11], 0, v[14:15]
	s_mov_b32 m0, s4
	v_readfirstlane_b32 s4, v12
	global_load_lds_dwordx4 v[10:11], off
	v_lshl_add_u64 v[10:11], v[10:11], 0, s[6:7]
	s_mov_b32 m0, s4
	s_nop 0
	global_load_lds_dwordx4 v[10:11], off
	s_waitcnt lgkmcnt(0)
	s_barrier
	v_lshlrev_b32_e32 v10, 2, v0
	v_and_b32_e32 v94, 12, v10
	v_or_b32_e32 v120, v94, v61
	v_bitop3_b32 v10, v124, v94, v61 bitop3:0x1e
	v_lshl_or_b32 v14, v10, 4, v18
	v_bitop3_b32 v10, v124, v120, 1 bitop3:0x36
	v_lshl_or_b32 v19, v10, 4, v18
	s_load_dwordx4 s[4:7], s[0:1], 0x20
	s_load_dwordx2 s[12:13], s[0:1], 0x38
	ds_read_b128 v[10:13], v14
	ds_read_b128 v[62:65], v14 offset:8192
	ds_read_b128 v[14:17], v19
	ds_read_b128 v[66:69], v19 offset:8192
	v_bitop3_b32 v19, v124, v120, 4 bitop3:0x36
	v_lshl_or_b32 v19, v19, 4, v18
	v_bitop3_b32 v20, v124, v120, 5 bitop3:0x36
	v_lshl_or_b32 v20, v20, 4, v18
	ds_read_b128 v[70:73], v19
	ds_read_b128 v[78:81], v19 offset:8192
	ds_read_b128 v[74:77], v20
	ds_read_b128 v[82:85], v20 offset:8192
	v_bitop3_b32 v19, v124, v120, 8 bitop3:0x36
	v_lshl_or_b32 v19, v19, 4, v18
	v_bitop3_b32 v20, v124, v120, 9 bitop3:0x36
	v_lshl_or_b32 v20, v20, 4, v18
	ds_read_b128 v[86:89], v19
	ds_read_b128 v[104:107], v19 offset:8192
	ds_read_b128 v[90:93], v20
	ds_read_b128 v[108:111], v20 offset:8192
	v_bitop3_b32 v19, v124, v120, 12 bitop3:0x36
	v_lshl_or_b32 v19, v19, 4, v18
	v_bitop3_b32 v20, v124, v120, 13 bitop3:0x36
	v_lshl_or_b32 v18, v20, 4, v18
	ds_read_b128 v[126:129], v19
	ds_read_b128 v[134:137], v19 offset:8192
	ds_read_b128 v[130:133], v18
	ds_read_b128 v[138:141], v18 offset:8192
	v_mov_b32_e32 v103, 0x7f
	v_lshlrev_b32_e32 v58, 7, v99
	v_or_b32_e32 v122, 0x18000, v117
	s_waitcnt vmcnt(8) lgkmcnt(0)
	v_mfma_scale_f32_32x32x64_f8f6f4 v[18:33], v[2:9], v[10:17], 0, v103, v103 op_sel_hi:[0,0,0]
	v_lshlrev_b32_e32 v125, 3, v119
	v_or_b32_e32 v123, 0x1a000, v117
	v_mfma_scale_f32_32x32x64_f8f6f4 v[2:17], v[2:9], v[62:69], 0, v103, v103 op_sel_hi:[0,0,0]
	v_and_b32_e32 v62, 12, v95
	v_mfma_scale_f32_32x32x64_f8f6f4 v[18:33], v[50:57], v[70:77], v[18:33], v103, v103 op_sel_hi:[0,0,0]
	v_mfma_scale_f32_32x32x64_f8f6f4 v[2:17], v[50:57], v[78:85], v[2:17], v103, v103 op_sel_hi:[0,0,0]
	v_lshl_add_u64 v[50:51], s[10:11], 0, v[58:59]
	v_lshlrev_b32_e32 v58, 4, v119
	v_lshl_add_u64 v[54:55], v[50:51], 0, v[58:59]
	global_load_dwordx4 v[50:53], v[54:55], off
	s_brev_b32 s10, 60
	v_lshlrev_b32_e32 v58, 6, v0
	v_and_b32_e32 v58, 0x4000, v58
	v_or3_b32 v63, v122, v58, v125
	v_or3_b32 v58, v123, v58, v125
	v_mfma_scale_f32_32x32x64_f8f6f4 v[18:33], v[42:49], v[86:93], v[18:33], v103, v103 op_sel_hi:[0,0,0]
	v_mfma_scale_f32_32x32x64_f8f6f4 v[2:17], v[42:49], v[104:111], v[2:17], v103, v103 op_sel_hi:[0,0,0]
	global_load_dwordx4 v[42:45], v[54:55], off offset:32
	global_load_dwordx4 v[46:49], v[54:55], off offset:64
	s_nop 0
	global_load_dwordx4 v[54:57], v[54:55], off offset:96
	v_mfma_scale_f32_32x32x64_f8f6f4 v[2:17], v[34:41], v[134:141], v[2:17], v103, v103 op_sel_hi:[0,0,0]
	v_mfma_scale_f32_32x32x64_f8f6f4 v[18:33], v[34:41], v[126:133], v[18:33], v103, v103 op_sel_hi:[0,0,0]
	s_waitcnt vmcnt(0)
	s_nop 15
	s_nop 1
	v_fma_f32 v2, v2, s10, v50
	v_fma_f32 v3, v3, s10, v51
	v_fma_f32 v4, v4, s10, v52
	v_fma_f32 v5, v5, s10, v53
	v_cvt_pk_f16_f32 v2, v2, v3
	v_cvt_pk_f16_f32 v3, v4, v5
	v_bitop3_b32 v4, v95, v120, 12 bitop3:0x6c
	v_pk_fma_f32 v[18:19], v[18:19], s[10:11], v[50:51] op_sel_hi:[1,0,1]
	v_pk_fma_f32 v[20:21], v[20:21], s[10:11], v[52:53] op_sel_hi:[1,0,1]
	v_lshlrev_b32_e32 v4, 4, v4
	v_cvt_pk_f16_f32 v18, v18, v19
	v_cvt_pk_f16_f32 v19, v20, v21
	v_or_b32_e32 v5, v63, v4
	v_or_b32_e32 v4, v58, v4
	ds_write_b64 v5, v[18:19]
	ds_write_b64 v4, v[2:3]
	v_pk_fma_f32 v[2:3], v[22:23], s[10:11], v[42:43] op_sel_hi:[1,0,1]
	v_pk_fma_f32 v[4:5], v[6:7], s[10:11], v[42:43] op_sel_hi:[1,0,1]
	v_pk_fma_f32 v[6:7], v[24:25], s[10:11], v[44:45] op_sel_hi:[1,0,1]
	v_cvt_pk_f16_f32 v2, v2, v3
	v_cvt_pk_f16_f32 v3, v6, v7
	v_pk_fma_f32 v[6:7], v[8:9], s[10:11], v[44:45] op_sel_hi:[1,0,1]
	v_cvt_pk_f16_f32 v4, v4, v5
	v_cvt_pk_f16_f32 v5, v6, v7
	v_bitop3_b32 v6, v62, v120, 1 bitop3:0x36
	v_lshlrev_b32_e32 v6, 4, v6
	v_or_b32_e32 v7, v63, v6
	ds_write_b64 v7, v[2:3]
	v_or_b32_e32 v2, v58, v6
	ds_write_b64 v2, v[4:5]
	v_pk_fma_f32 v[2:3], v[26:27], s[10:11], v[46:47] op_sel_hi:[1,0,1]
	v_pk_fma_f32 v[6:7], v[28:29], s[10:11], v[48:49] op_sel_hi:[1,0,1]
	v_cvt_pk_f16_f32 v2, v2, v3
	v_pk_fma_f32 v[4:5], v[10:11], s[10:11], v[46:47] op_sel_hi:[1,0,1]
	v_cvt_pk_f16_f32 v3, v6, v7
	v_pk_fma_f32 v[6:7], v[12:13], s[10:11], v[48:49] op_sel_hi:[1,0,1]
	v_cvt_pk_f16_f32 v4, v4, v5
	v_cvt_pk_f16_f32 v5, v6, v7
	v_bitop3_b32 v6, v62, v120, 2 bitop3:0x36
	v_lshlrev_b32_e32 v6, 4, v6
	v_or_b32_e32 v7, v63, v6
	ds_write_b64 v7, v[2:3]
	v_or_b32_e32 v2, v58, v6
	ds_write_b64 v2, v[4:5]
	v_pk_fma_f32 v[2:3], v[30:31], s[10:11], v[54:55] op_sel_hi:[1,0,1]
	v_pk_fma_f32 v[6:7], v[32:33], s[10:11], v[56:57] op_sel_hi:[1,0,1]
	v_cvt_pk_f16_f32 v2, v2, v3
	v_pk_fma_f32 v[4:5], v[14:15], s[10:11], v[54:55] op_sel_hi:[1,0,1]
	v_cvt_pk_f16_f32 v3, v6, v7
	v_pk_fma_f32 v[6:7], v[16:17], s[10:11], v[56:57] op_sel_hi:[1,0,1]
	v_cvt_pk_f16_f32 v4, v4, v5
	v_cvt_pk_f16_f32 v5, v6, v7
	v_bitop3_b32 v6, v62, v120, 3 bitop3:0x36
	v_lshlrev_b32_e32 v6, 4, v6
	v_or_b32_e32 v7, v63, v6
	ds_write_b64 v7, v[2:3]
	v_or_b32_e32 v2, v58, v6
	ds_write_b64 v2, v[4:5]
	s_waitcnt lgkmcnt(0)
	s_barrier
	v_lshrrev_b32_e32 v27, 8, v0
	v_lshrrev_b32_e32 v3, 3, v0
	v_and_b32_e32 v3, 16, v3
	v_mul_u32_u24_e32 v28, 0x60, v27
	v_lshlrev_b32_e32 v26, 5, v27
	v_or_b32_e32 v146, v3, v100
	v_or_b32_e32 v147, v28, v100
	v_or_b32_e32 v4, v146, v26
	v_lshlrev_b32_e32 v209, 2, v4
	v_add_u32_e32 v209, 0x27800, v209
	v_lshlrev_b32_e32 v4, 8, v4
	v_or_b32_e32 v5, 0x18000, v4
	v_bitop3_b32 v11, v101, v120, 12 bitop3:0x36
	v_or_b32_e32 v95, 0x1c000, v4
	v_lshlrev_b32_e32 v29, 3, v101
	v_bitop3_b32 v6, v101, v94, v61 bitop3:0x1e
	v_bitop3_b32 v8, v101, v120, 4 bitop3:0x36
	v_bitop3_b32 v10, v101, v120, 8 bitop3:0x36
	v_lshlrev_b32_e32 v94, 4, v11
	v_lshlrev_b32_e32 v6, 4, v6
	v_lshlrev_b32_e32 v8, 4, v8
	v_lshlrev_b32_e32 v58, 4, v10
	v_or_b32_e32 v7, v5, v6
	v_or_b32_e32 v9, v5, v8
	v_or_b32_e32 v10, v5, v58
	v_or_b32_e32 v5, v5, v94
	v_or_b32_e32 v6, v95, v6
	v_or_b32_e32 v60, v95, v8
	ds_read_b128 v[22:25], v7
	ds_read_b128 v[18:21], v9
	ds_read_b128 v[14:17], v10
	ds_read_b128 v[10:13], v5
	ds_read_b128 v[6:9], v6
	ds_read_b128 v[2:5], v60
	v_bfe_u32 v103, v0, 6, 1
	s_movk_i32 s5, 0x2000
	v_mad_u32_u24 v44, v103, 48, v147
	v_lshlrev_b32_e32 v60, 8, v44
	v_lshlrev_b32_e32 v44, 2, v44
	v_or_b32_e32 v35, v95, v58
	v_lshlrev_b32_e32 v58, 14, v99
	v_and_b32_e32 v44, 12, v44
	v_or_b32_e32 v56, v44, v61
	v_bitop3_b32 v44, v101, v44, v61 bitop3:0x1e
	v_lshl_add_u64 v[32:33], s[8:9], 0, v[58:59]
	v_lshlrev_b32_e32 v58, 4, v98
	v_or_b32_e32 v36, v95, v94
	v_lshl_add_u64 v[88:89], v[32:33], 0, v[58:59]
	v_lshl_or_b32 v57, v44, 4, v60
	ds_read_b128 v[40:43], v35
	ds_read_b128 v[106:109], v36
	s_load_dword s4, s[6:7], 0x0
	ds_read_b128 v[44:47], v57
	v_bitop3_b32 v48, v101, v56, 4 bitop3:0x36
	v_lshl_or_b32 v62, v48, 4, v60
	ds_read_b128 v[48:51], v62
	v_bitop3_b32 v52, v101, v56, 8 bitop3:0x36
	v_lshl_or_b32 v63, v52, 4, v60
	ds_read_b128 v[52:55], v63
	s_waitcnt lgkmcnt(0)
	v_mfma_f32_16x16x32_f16 v[44:47], v[44:47], v[22:25], 0
	v_bitop3_b32 v64, v101, v56, 12 bitop3:0x36
	ds_read_b128 v[56:59], v57 offset:49152
	v_lshl_or_b32 v60, v64, 4, v60
	v_mfma_f32_16x16x32_f16 v[44:47], v[48:51], v[18:21], v[44:47]
	ds_read_b128 v[68:71], v60
	ds_read_b128 v[72:75], v62 offset:49152
	v_mad_u32_u24 v104, v103, 3, 1
	v_lshlrev_b32_e32 v132, 4, v104
	v_mfma_f32_16x16x32_f16 v[44:47], v[52:55], v[14:17], v[44:47]
	v_add_u32_e32 v52, v132, v147
	ds_read_b128 v[76:79], v63 offset:49152
	ds_read_b128 v[80:83], v60 offset:49152
	s_waitcnt lgkmcnt(3)
	v_mfma_f32_16x16x32_f16 v[44:47], v[68:71], v[10:13], v[44:47]
	v_lshlrev_b32_e32 v60, 8, v52
	v_lshlrev_b32_e32 v52, 2, v52
	v_and_b32_e32 v52, 12, v52
	v_mfma_f32_16x16x32_f16 v[44:47], v[56:59], v[6:9], v[44:47]
	v_or_b32_e32 v62, v52, v61
	v_bitop3_b32 v52, v101, v52, v61 bitop3:0x1e
	v_lshl_or_b32 v63, v52, 4, v60
	s_waitcnt lgkmcnt(2)
	v_mfma_f32_16x16x32_f16 v[44:47], v[72:75], v[2:5], v[44:47]
	ds_read_b128 v[52:55], v63
	v_bitop3_b32 v56, v101, v62, 4 bitop3:0x36
	v_lshl_or_b32 v84, v56, 4, v60
	s_waitcnt lgkmcnt(2)
	v_mfma_f32_16x16x32_f16 v[44:47], v[76:79], v[40:43], v[44:47]
	ds_read_b128 v[56:59], v84
	v_bitop3_b32 v68, v101, v62, 8 bitop3:0x36
	v_lshl_or_b32 v85, v68, 4, v60
	s_waitcnt lgkmcnt(2)
	v_mfma_f32_16x16x32_f16 v[110:113], v[80:83], v[106:109], v[44:47]
	ds_read_b128 v[68:71], v63 offset:49152
	v_bitop3_b32 v62, v101, v62, 12 bitop3:0x36
	v_lshl_or_b32 v60, v62, 4, v60
	ds_read_b128 v[44:47], v85
	s_waitcnt lgkmcnt(3)
	v_mfma_f32_16x16x32_f16 v[52:55], v[52:55], v[22:25], 0
	ds_read_b128 v[72:75], v60
	ds_read_b128 v[76:79], v84 offset:49152
	v_mad_u32_u24 v105, v103, 3, 2
	v_lshlrev_b32_e32 v133, 4, v105
	s_waitcnt lgkmcnt(4)
	v_mfma_f32_16x16x32_f16 v[52:55], v[56:59], v[18:21], v[52:55]
	ds_read_b128 v[56:59], v85 offset:49152
	v_add_co_u32_e32 v114, vcc, s15, v88
	s_waitcnt lgkmcnt(3)
	v_mfma_f32_16x16x32_f16 v[44:47], v[44:47], v[14:17], v[52:55]
	v_addc_co_u32_e32 v115, vcc, 0, v89, vcc
	s_waitcnt lgkmcnt(2)
	v_mfma_f32_16x16x32_f16 v[44:47], v[72:75], v[10:13], v[44:47]
	ds_read_b128 v[52:55], v60 offset:49152
	v_add_u32_e32 v60, v133, v147
	v_lshlrev_b32_e32 v72, 8, v60
	v_lshlrev_b32_e32 v60, 2, v60
	v_mfma_f32_16x16x32_f16 v[44:47], v[68:71], v[6:9], v[44:47]
	v_and_b32_e32 v60, 12, v60
	v_or_b32_e32 v68, v60, v61
	v_bitop3_b32 v60, v101, v60, v61 bitop3:0x1e
	v_lshl_or_b32 v69, v60, 4, v72
	s_waitcnt lgkmcnt(2)
	v_mfma_f32_16x16x32_f16 v[44:47], v[76:79], v[2:5], v[44:47]
	ds_read_b128 v[60:63], v69
	v_bitop3_b32 v70, v101, v68, 4 bitop3:0x36
	v_lshl_or_b32 v70, v70, 4, v72
	s_waitcnt lgkmcnt(2)
	v_mfma_f32_16x16x32_f16 v[44:47], v[56:59], v[40:43], v[44:47]
	ds_read_b128 v[56:59], v70
	v_bitop3_b32 v71, v101, v68, 8 bitop3:0x36
	v_lshl_or_b32 v71, v71, 4, v72
	s_waitcnt lgkmcnt(1)
	v_mfma_f32_16x16x32_f16 v[22:25], v[60:63], v[22:25], 0
	v_bitop3_b32 v60, v101, v68, 12 bitop3:0x36
	v_lshl_or_b32 v68, v60, 4, v72
	ds_read_b32 v210, v209
	v_mfma_f32_16x16x32_f16 v[126:129], v[52:55], v[106:109], v[44:47]
	s_nop 2
	ds_read_b128 v[44:47], v71
	ds_read_b128 v[52:55], v69 offset:49152
	ds_read_b128 v[60:63], v70 offset:49152
	s_waitcnt lgkmcnt(4)
	v_mfma_f32_16x16x32_f16 v[18:21], v[56:59], v[18:21], v[22:25]
	ds_read_b128 v[56:59], v71 offset:49152
	s_nop 1
	ds_read_b128 v[22:25], v68
	s_waitcnt lgkmcnt(4)
	v_mfma_f32_16x16x32_f16 v[14:17], v[44:47], v[14:17], v[18:21]
	v_add_co_u32_e32 v44, vcc, s5, v88
	s_movk_i32 s5, 0x3000
	s_nop 0
	ds_read_b128 v[18:21], v68 offset:49152
	s_waitcnt lgkmcnt(1)
	v_mfma_f32_16x16x32_f16 v[10:13], v[22:25], v[10:13], v[14:17]
	v_addc_co_u32_e32 v45, vcc, 0, v89, vcc
	v_mfma_f32_16x16x32_f16 v[6:9], v[52:55], v[6:9], v[10:13]
	v_mov_b32_e32 v13, 0xff61b1e6
	v_mfma_f32_16x16x32_f16 v[2:5], v[60:63], v[2:5], v[6:9]
	s_nop 2
	v_add_co_u32_e32 v6, vcc, s5, v88
	v_mfma_f32_16x16x32_f16 v[2:5], v[56:59], v[40:43], v[2:5]
	s_nop 0
	v_addc_co_u32_e32 v7, vcc, 0, v89, vcc
	s_waitcnt lgkmcnt(0)
	v_mfma_f32_16x16x32_f16 v[16:19], v[18:21], v[106:109], v[2:5]
	s_mov_b32 s5, 0xff61b1e6
	s_nop 0
	v_or_b32_e32 v3, s14, v146
	v_mov_b32_e32 v4, 0x7df
	v_med3_u32 v3, v3, 32, v4
	v_or_b32_e32 v4, v97, v102
	v_sub_u32_e32 v3, v4, v3
	v_add_f32_e32 v2, s4, v210
	v_add_u32_e32 v3, 32, v3
	v_mad_u32_u24 v4, v103, 48, v3
	s_movk_i32 s4, 0x41
	v_add_f32_e32 v5, v2, v110
	v_mul_f32_e32 v5, 0x3db8aa3b, v5
	v_cmp_gt_u32_e32 vcc, s4, v4
	v_add_u32_e32 v6, 1, v4
	v_add_f32_e32 v7, v2, v111
	v_cndmask_b32_e32 v5, v13, v5, vcc
	v_mul_f32_e32 v7, 0x3db8aa3b, v7
	v_cmp_gt_u32_e32 vcc, s4, v6
	v_add_u32_e32 v8, 2, v4
	v_add_f32_e32 v9, v2, v112
	v_cndmask_b32_e32 v6, v13, v7, vcc
	v_mul_f32_e32 v9, 0x3db8aa3b, v9
	v_cmp_gt_u32_e32 vcc, s4, v8
	v_add_u32_e32 v4, 3, v4
	v_max3_f32 v7, v5, s5, v6
	v_cndmask_b32_e32 v8, v13, v9, vcc
	v_add_f32_e32 v9, v2, v113
	v_mul_f32_e32 v9, 0x3db8aa3b, v9
	v_cmp_gt_u32_e32 vcc, s4, v4
	v_add_u32_e32 v11, v3, v132
	v_add_f32_e32 v12, v2, v127
	v_cndmask_b32_e32 v10, v13, v9, vcc
	v_max3_f32 v4, v7, v8, v10
	v_add_f32_e32 v7, v2, v126
	v_mul_f32_e32 v7, 0x3db8aa3b, v7
	v_cmp_gt_u32_e32 vcc, s4, v11
	v_add_u32_e32 v9, 1, v11
	v_mul_f32_e32 v12, 0x3db8aa3b, v12
	v_cndmask_b32_e32 v7, v13, v7, vcc
	v_cmp_gt_u32_e32 vcc, s4, v9
	v_add_f32_e32 v14, v2, v128
	v_mul_f32_e32 v14, 0x3db8aa3b, v14
	v_cndmask_b32_e32 v9, v13, v12, vcc
	v_add_u32_e32 v12, 2, v11
	v_cmp_gt_u32_e32 vcc, s4, v12
	v_add_u32_e32 v11, 3, v11
	v_add_u32_e32 v3, v3, v133
	v_cndmask_b32_e32 v12, v13, v14, vcc
	v_add_f32_e32 v14, v2, v129
	v_mul_f32_e32 v14, 0x3db8aa3b, v14
	v_cmp_gt_u32_e32 vcc, s4, v11
	v_add_f32_e32 v11, v2, v16
	v_mul_f32_e32 v11, 0x3db8aa3b, v11
	v_cndmask_b32_e32 v15, v13, v14, vcc
	v_cmp_gt_u32_e32 vcc, s4, v3
	v_add_u32_e32 v14, 1, v3
	v_add_f32_e32 v16, v2, v17
	v_cndmask_b32_e32 v11, v13, v11, vcc
	v_mul_f32_e32 v16, 0x3db8aa3b, v16
	v_cmp_gt_u32_e32 vcc, s4, v14
	v_add_f32_e32 v17, v2, v18
	v_max3_f32 v4, v4, v7, v9
	v_cndmask_b32_e32 v14, v13, v16, vcc
	v_add_u32_e32 v16, 2, v3
	v_mul_f32_e32 v17, 0x3db8aa3b, v17
	v_cmp_gt_u32_e32 vcc, s4, v16
	v_add_u32_e32 v3, 3, v3
	v_add_f32_e32 v2, v2, v19
	v_max3_f32 v4, v4, v12, v15
	v_cndmask_b32_e32 v16, v13, v17, vcc
	v_mul_f32_e32 v2, 0x3db8aa3b, v2
	v_cmp_gt_u32_e32 vcc, s4, v3
	v_max3_f32 v4, v4, v11, v14
	v_lshlrev_b32_e32 v126, 5, v99
	v_cndmask_b32_e32 v17, v13, v2, vcc
	v_max3_f32 v2, v4, v16, v17
	v_mov_b32_e32 v3, v2
	v_lshlrev_b32_e32 v127, 2, v119
	v_lshrrev_b32_e32 v4, 7, v0
	v_cmp_gt_u32_e32 vcc, 16, v98
	v_permlane16_swap_b32_e32 v3, v2
	v_max_f32_e32 v2, v2, v3
	v_mov_b32_e32 v3, v2
	s_nop 1
	v_permlane32_swap_b32_e32 v3, v2
	v_max_f32_e32 v13, v2, v3
	v_and_b32_e32 v2, 0x180, v0
	v_or_b32_e32 v2, 0x23400, v2
	v_lshlrev_b32_e32 v3, 2, v100
	s_and_saveexec_b64 s[4:5], vcc
	v_lshlrev_b32_e32 v18, 6, v103
	v_add3_u32 v18, v2, v18, v3
	ds_write_b32 v18, v13
	s_or_b64 exec, exec, s[4:5]
	v_lshlrev_b32_e32 v18, 4, v103
	v_bitop3_b32 v19, v18, 16, v100 bitop3:0x36
	v_lshl_add_u32 v2, v19, 2, v2
	s_waitcnt lgkmcnt(0)
	s_barrier
	v_lshlrev_b32_e32 v232, 14, v99
	v_lshl_or_b32 v232, v98, 4, v232
	v_add_u32_e32 v233, 0x1000, v232
	v_add_u32_e32 v234, 0x2000, v232
	v_add_u32_e32 v235, 0x3000, v232
	ds_read_b32 v19, v2
	v_max_f32_e32 v13, v13, v13
	v_mul_u32_u24_e32 v20, 0xd00, v4
	s_load_dwordx2 s[0:1], s[0:1], 0x30
	v_or_b32_e32 v2, 1, v124
	s_waitcnt lgkmcnt(0)
	v_max_f32_e32 v19, v19, v19
	v_max_f32_e32 v19, v13, v19
	v_sub_f32_e32 v5, v5, v19
	v_exp_f32_e32 v5, v5
	global_load_dwordx4 v[36:39], v232, s[20:21]
	v_sub_f32_e32 v6, v6, v19
	v_exp_f32_e32 v6, v6
	v_sub_f32_e32 v8, v8, v19
	v_mul_u32_u24_e32 v13, 0xd0, v100
	v_exp_f32_e32 v8, v8
	v_sub_f32_e32 v10, v10, v19
	v_add3_u32 v20, v13, v20, v29
	v_exp_f32_e32 v10, v10
	v_or_b32_e32 v22, 0x20000, v20
	v_add_f32_e32 v20, 0, v5
	global_load_dwordx4 v[32:35], v232, s[20:21] offset:1024
	v_add_f32_e32 v20, v20, v6
	v_add_f32_e32 v20, v20, v8
	v_add_f32_e32 v23, v20, v10
	v_cvt_pk_f16_f32 v21, v8, v10
	v_cvt_pk_f16_f32 v20, v5, v6
	v_mad_u32_u24 v5, v103, s16, v22
	ds_write_b64 v5, v[20:21]
	v_sub_f32_e32 v5, v7, v19
	v_exp_f32_e32 v5, v5
	v_sub_f32_e32 v6, v9, v19
	global_load_dwordx4 v[64:67], v232, s[20:21] offset:2048
	v_exp_f32_e32 v6, v6
	v_sub_f32_e32 v7, v12, v19
	v_exp_f32_e32 v7, v7
	v_sub_f32_e32 v8, v15, v19
	v_exp_f32_e32 v8, v8
	v_sub_f32_e32 v10, v11, v19
	v_add_f32_e32 v9, v23, v5
	v_exp_f32_e32 v10, v10
	v_sub_f32_e32 v11, v14, v19
	v_add_f32_e32 v9, v9, v6
	global_load_dwordx4 v[48:51], v232, s[20:21] offset:3072
	v_exp_f32_e32 v11, v11
	v_sub_f32_e32 v12, v16, v19
	v_add_f32_e32 v9, v9, v7
	v_exp_f32_e32 v12, v12
	v_sub_f32_e32 v14, v17, v19
	v_add_f32_e32 v9, v9, v8
	v_exp_f32_e32 v14, v14
	v_add_f32_e32 v9, v9, v10
	v_add_f32_e32 v9, v9, v11
	v_add_f32_e32 v9, v9, v12
	v_add_f32_e32 v9, v9, v14
	v_mov_b32_e32 v15, v9
	v_cvt_pk_f16_f32 v7, v7, v8
	v_cvt_pk_f16_f32 v6, v5, v6
	v_lshl_add_u32 v5, v104, 5, v22
	ds_write_b64 v5, v[6:7]
	v_permlane16_swap_b32_e32 v15, v9
	v_add_f32_e32 v5, v9, v15
	v_mov_b32_e32 v6, v5
	s_movk_i32 s7, 0xd00
	s_mov_b32 s6, 0x20000
	v_cvt_pk_f16_f32 v9, v12, v14
	v_cvt_pk_f16_f32 v8, v10, v11
	v_lshl_add_u32 v7, v105, 5, v22
	ds_write_b64 v7, v[8:9]
	v_permlane32_swap_b32_e32 v6, v5
	s_and_saveexec_b64 s[4:5], vcc
	s_cbranch_execz .LBB1_4
	v_lshlrev_b32_e32 v4, 5, v4
	v_or_b32_e32 v7, v18, v100
	v_lshlrev_b32_e32 v4, 2, v4
	v_lshlrev_b32_e32 v7, 2, v7
	s_mov_b32 s8, 0x23600
	v_add3_u32 v4, v7, v4, s8
	v_add_f32_e32 v5, v5, v6
	ds_write_b32 v4, v5
.LBB1_4:
	s_or_b64 exec, exec, s[4:5]
	v_lshl_or_b32 v4, v27, 1, v96
	v_lshl_or_b32 v3, v4, 7, v3
	v_or_b32_e32 v5, 0x23600, v3
	v_or_b32_e32 v3, 0x23640, v3
	s_waitcnt lgkmcnt(0)
	s_barrier
	ds_read_b32 v5, v5
	ds_read_b32 v3, v3
	v_mad_u32_u24 v4, v4, s7, v13
	v_lshl_add_u32 v4, v119, 4, v4
	v_or_b32_e32 v6, 0x20000, v4
	ds_read_b128 v[16:19], v6
	s_waitcnt lgkmcnt(1)
	v_add_f32_e32 v3, v5, v3
	v_add_u32_e32 v5, 0x20020, v4
	v_add_u32_e32 v6, 0x20040, v4
	ds_read_b128 v[112:115], v5
	ds_read_b128 v[108:111], v6
	global_load_dwordx4 v[84:87], v233, s[20:21] offset:1024
	v_add_u32_e32 v5, 0x20060, v4
	v_add_u32_e32 v6, 0x20080, v4
	v_lshlrev_b32_e32 v7, 1, v101
	ds_read_b128 v[104:107], v5
	ds_read_b128 v[96:99], v6
	v_lshrrev_b32_e32 v5, 2, v100
	v_or_b32_e32 v6, v28, v125
	v_and_b32_e32 v7, 2, v7
	v_bfe_u32 v8, v0, 1, 1
	v_and_b32_e32 v164, 8, v121
	v_bfe_i32 v9, v0, 7, 1
	v_or3_b32 v8, v8, v7, v164
	global_load_dwordx4 v[80:83], v233, s[20:21] offset:2048
	v_and_b32_e32 v0, 12, v0
	v_add_lshl_u32 v10, v6, v5, 8
	v_or_b32_e32 v5, v6, v5
	v_and_b32_e32 v9, 0xc000, v9
	v_lshlrev_b32_e32 v12, 8, v5
	v_bitop3_b32 v5, v0, v8, v124 bitop3:0x36
	v_lshl_or_b32 v13, v5, 4, v9
	v_bitop3_b32 v6, v0, v8, v2 bitop3:0x36
	v_or_b32_e32 v15, 0x1000, v12
	v_lshl_or_b32 v14, v6, 4, v9
	v_add_u32_e32 v7, v13, v15
	v_or_b32_e32 v24, 0x1400, v12
	global_load_dwordx4 v[92:95], v233, s[20:21]
	v_or_b32_e32 v20, v7, v1
	v_add_u32_e32 v7, v14, v24
	v_add_u32_e32 v25, 0x2000, v10
	v_add_u32_e32 v5, v13, v12
	v_add_u32_e32 v6, v14, v12
	v_or_b32_e32 v22, v7, v1
	v_add_u32_e32 v7, v13, v25
	v_add_u32_e32 v150, 0x3000, v10
	v_or_b32_e32 v8, 4, v8
	v_add_u32_e32 v4, 0x200a0, v4
	v_or_b32_e32 v5, v5, v1
	v_or_b32_e32 v6, v6, v1
	global_load_dwordx4 v[76:79], v234, s[20:21]
	v_or_b32_e32 v27, v7, v1
	v_add_u32_e32 v31, v13, v150
	v_add_u32_e32 v151, 0x3400, v10
	v_bitop3_b32 v124, v0, v8, v124 bitop3:0x36
	v_bitop3_b32 v0, v0, v8, v2 bitop3:0x36
	ds_read_b128 v[100:103], v4
	ds_read_b64_tr_b16 v[4:5], v5
	ds_read_b64_tr_b16 v[6:7], v6 offset:1024
	ds_read_b64_tr_b16 v[20:21], v20
	ds_read_b64_tr_b16 v[22:23], v22
	ds_read_b64_tr_b16 v[28:29], v27
	v_add_u32_e32 v27, 0x2400, v10
	global_load_dwordx4 v[72:75], v234, s[20:21] offset:1024
	v_or_b32_e32 v128, v31, v1
	v_add_u32_e32 v31, v14, v151
	v_add_u32_e32 v152, 0x4000, v10
	v_add_u32_e32 v158, 0x4400, v10
	v_lshl_or_b32 v124, v124, 4, v9
	v_lshl_or_b32 v0, v0, 4, v9
	v_add_u32_e32 v11, 0x5000, v10
	v_add_u32_e32 v30, v14, v27
	v_or_b32_e32 v130, v31, v1
	v_add_u32_e32 v31, v13, v152
	v_add_u32_e32 v134, v14, v158
	v_add_u32_e32 v10, 0x5400, v10
	global_load_dwordx4 v[68:71], v234, s[20:21] offset:2048
	v_add_u32_e32 v135, v124, v12
	v_add_u32_e32 v2, v0, v12
	v_add_u32_e32 v8, v124, v15
	v_or_b32_e32 v30, v30, v1
	v_or_b32_e32 v132, v31, v1
	v_or_b32_e32 v134, v134, v1
	v_add_u32_e32 v13, v13, v11
	v_add_u32_e32 v14, v14, v10
	v_or_b32_e32 v140, v135, v1
	v_or_b32_e32 v2, v2, v1
	v_or_b32_e32 v8, v8, v1
	v_add_u32_e32 v9, v0, v24
	global_load_dwordx4 v[52:55], v234, s[20:21] offset:3072
	v_add_u32_e32 v12, v124, v25
	ds_read_b64_tr_b16 v[30:31], v30
	ds_read_b64_tr_b16 v[128:129], v128
	ds_read_b64_tr_b16 v[130:131], v130
	ds_read_b64_tr_b16 v[132:133], v132
	v_or_b32_e32 v13, v13, v1
	v_or_b32_e32 v14, v14, v1
	ds_read_b64_tr_b16 v[134:135], v134
	ds_read_b64_tr_b16 v[136:137], v13
	ds_read_b64_tr_b16 v[138:139], v14
	ds_read_b64_tr_b16 v[140:141], v140
	v_or_b32_e32 v9, v9, v1
	global_load_dwordx4 v[88:91], v233, s[20:21] offset:3072
	v_or_b32_e32 v12, v12, v1
	ds_read_b64_tr_b16 v[142:143], v2 offset:1024
	ds_read_b64_tr_b16 v[144:145], v8
	ds_read_b64_tr_b16 v[146:147], v9
	ds_read_b64_tr_b16 v[148:149], v12
	v_add_u32_e32 v2, v0, v27
	v_add_u32_e32 v8, v124, v150
	v_or_b32_e32 v2, v2, v1
	v_or_b32_e32 v8, v8, v1
	v_add_u32_e32 v9, v0, v151
	v_add_u32_e32 v12, v124, v152
	v_or_b32_e32 v9, v9, v1
	global_load_dwordx4 v[60:63], v235, s[20:21]
	v_or_b32_e32 v12, v12, v1
	ds_read_b64_tr_b16 v[150:151], v2
	ds_read_b64_tr_b16 v[152:153], v8
	ds_read_b64_tr_b16 v[154:155], v9
	ds_read_b64_tr_b16 v[156:157], v12
	v_add_u32_e32 v2, v0, v158
	v_add_u32_e32 v8, v124, v11
	v_add_u32_e32 v0, v0, v10
	v_or_b32_e32 v2, v2, v1
	v_or_b32_e32 v8, v8, v1
	v_or_b32_e32 v0, v0, v1
	v_div_scale_f32 v1, s[8:9], v3, v3, 1.0
	global_load_dwordx4 v[56:59], v235, s[20:21] offset:1024
	v_rcp_f32_e32 v9, v1
	ds_read_b64_tr_b16 v[158:159], v2
	ds_read_b64_tr_b16 v[160:161], v8
	ds_read_b64_tr_b16 v[162:163], v0
	s_mov_b32 s4, 0xc000
	s_movk_i32 s5, 0x4000
	v_fma_f32 v0, -v1, v9, 1.0
	v_fmac_f32_e32 v9, v0, v9
	v_div_scale_f32 v0, vcc, 1.0, v3, 1.0
	v_mul_f32_e32 v2, v0, v9
	v_fma_f32 v8, -v1, v2, v0
	v_fmac_f32_e32 v2, v8, v9
	global_load_dwordx4 v[44:47], v235, s[20:21] offset:2048
	v_fma_f32 v0, -v1, v2, v0
	v_div_fmas_f32 v0, v0, v9, v2
	v_div_fixup_f32 v124, v0, v3, 1.0
	s_waitcnt lgkmcnt(14)
	v_mfma_f32_32x32x16_f16 v[0:15], v[4:7], v[16:19], 0
	s_mov_b32 s7, 0x18000
	v_lshlrev_b32_e32 v172, 2, v126
	v_mov_b32_e32 v173, 0
	v_mfma_f32_32x32x16_f16 v[0:15], v[20:23], v[112:115], v[0:15]
	v_or_b32_e32 v20, v26, v116
	v_and_b32_e32 v21, 0x4000, v118
	global_load_dwordx4 v[40:43], v235, s[20:21] offset:3072
	v_lshl_or_b32 v20, v20, 8, v21
	v_bitop3_b32 v118, v121, v120, 8 bitop3:0x6c
	v_or3_b32 v121, v20, v125, s7
	v_mfma_f32_32x32x16_f16 v[0:15], v[28:31], v[108:111], v[0:15]
	v_mfma_f32_32x32x16_f16 v[0:15], v[128:131], v[104:107], v[0:15]
	v_mfma_f32_32x32x16_f16 v[0:15], v[132:135], v[96:99], v[0:15]
	s_waitcnt lgkmcnt(12)
	v_mfma_f32_32x32x16_f16 v[0:15], v[136:139], v[100:103], v[0:15]
	s_nop 11
	v_fma_mixlo_f16 v20, v124, v0, 0
	v_mov_b32_e32 v0, v1
	v_mov_b32_e32 v1, v2
	v_pk_mul_f32 v[0:1], v[124:125], v[0:1] op_sel_hi:[0,1]
	v_cvt_pk_f16_f32 v1, v0, v1
	v_pack_b32_f16 v0, v20, v1
	s_waitcnt lgkmcnt(10)
	v_mfma_f32_32x32x16_f16 v[16:31], v[140:143], v[16:19], 0
	v_fma_mixlo_f16 v2, v124, v3, 0
	v_alignbit_b32 v1, v2, v1, 16
	v_lshl_or_b32 v2, v118, 4, v121
	ds_write_b64 v2, v[0:1]
	v_mov_b32_e32 v0, v5
	v_mov_b32_e32 v1, v6
	v_pk_mul_f32 v[0:1], v[124:125], v[0:1] op_sel_hi:[0,1]
	s_waitcnt lgkmcnt(9)
	v_mfma_f32_32x32x16_f16 v[16:31], v[144:147], v[112:115], v[16:31]
	v_fma_mixlo_f16 v2, v124, v4, 0
	v_cvt_pk_f16_f32 v1, v0, v1
	v_pack_b32_f16 v0, v2, v1
	v_fma_mixlo_f16 v2, v124, v7, 0
	v_alignbit_b32 v1, v2, v1, 16
	v_bitop3_b32 v2, v164, v120, 1 bitop3:0x36
	v_lshl_or_b32 v2, v2, 4, v121
	s_waitcnt lgkmcnt(7)
	v_mfma_f32_32x32x16_f16 v[16:31], v[148:151], v[108:111], v[16:31]
	ds_write_b64 v2, v[0:1]
	v_mov_b32_e32 v0, v9
	v_mov_b32_e32 v1, v10
	v_mul_f32_e64 v0, v124, v0
	v_mul_f32_e64 v1, v124, v1
	v_fma_mixlo_f16 v2, v124, v8, 0
	v_cvt_pk_f16_f32 v1, v0, v1
	v_pack_b32_f16 v0, v2, v1
	s_waitcnt lgkmcnt(6)
	v_mfma_f32_32x32x16_f16 v[16:31], v[152:155], v[104:107], v[16:31]
	v_fma_mixlo_f16 v2, v124, v11, 0
	v_alignbit_b32 v1, v2, v1, 16
	v_bitop3_b32 v2, v164, v120, 2 bitop3:0x36
	v_lshl_or_b32 v2, v2, 4, v121
	ds_write_b64 v2, v[0:1]
	v_mov_b32_e32 v0, v13
	v_mov_b32_e32 v1, v14
	s_waitcnt lgkmcnt(5)
	v_mfma_f32_32x32x16_f16 v[16:31], v[156:159], v[96:99], v[16:31]
	v_mul_f32_e64 v0, v124, v0
	v_mul_f32_e64 v1, v124, v1
	v_fma_mixlo_f16 v2, v124, v12, 0
	v_cvt_pk_f16_f32 v1, v0, v1
	v_pack_b32_f16 v0, v2, v1
	v_fma_mixlo_f16 v2, v124, v15, 0
	v_alignbit_b32 v1, v2, v1, 16
	v_bitop3_b32 v2, v164, v120, 3 bitop3:0x36
	s_waitcnt lgkmcnt(3)
	v_mfma_f32_32x32x16_f16 v[16:31], v[160:163], v[100:103], v[16:31]
	v_lshl_or_b32 v2, v2, 4, v121
	ds_write_b64 v2, v[0:1]
	s_nop 9
	v_mov_b32_e32 v0, v17
	v_mov_b32_e32 v1, v18
	v_pk_mul_f32 v[0:1], v[124:125], v[0:1] op_sel_hi:[0,1]
	v_fma_mixlo_f16 v2, v124, v16, 0
	v_cvt_pk_f16_f32 v1, v0, v1
	v_pack_b32_f16 v0, v2, v1
	v_fma_mixlo_f16 v2, v124, v19, 0
	v_alignbit_b32 v1, v2, v1, 16
	v_bitop3_b32 v2, v164, v120, 4 bitop3:0x36
	v_lshl_or_b32 v2, v2, 4, v121
	ds_write_b64 v2, v[0:1]
	v_mov_b32_e32 v0, v21
	v_mov_b32_e32 v1, v22
	v_pk_mul_f32 v[0:1], v[124:125], v[0:1] op_sel_hi:[0,1]
	v_fma_mixlo_f16 v2, v124, v20, 0
	v_cvt_pk_f16_f32 v1, v0, v1
	v_pack_b32_f16 v0, v2, v1
	v_fma_mixlo_f16 v2, v124, v23, 0
	v_alignbit_b32 v1, v2, v1, 16
	v_bitop3_b32 v2, v164, v120, 5 bitop3:0x36
	v_lshl_or_b32 v2, v2, 4, v121
	ds_write_b64 v2, v[0:1]
	v_mov_b32_e32 v0, v25
	v_mov_b32_e32 v1, v26
	v_pk_mul_f32 v[0:1], v[124:125], v[0:1] op_sel_hi:[0,1]
	v_fma_mixlo_f16 v2, v124, v24, 0
	v_cvt_pk_f16_f32 v1, v0, v1
	v_pack_b32_f16 v0, v2, v1
	v_fma_mixlo_f16 v2, v124, v27, 0
	v_alignbit_b32 v1, v2, v1, 16
	v_bitop3_b32 v2, v164, v120, 6 bitop3:0x36
	v_lshl_or_b32 v2, v2, 4, v121
	ds_write_b64 v2, v[0:1]
	v_mov_b32_e32 v0, v29
	v_mov_b32_e32 v1, v30
	v_pk_mul_f32 v[0:1], v[124:125], v[0:1] op_sel_hi:[0,1]
	v_fma_mixlo_f16 v2, v124, v28, 0
	v_cvt_pk_f16_f32 v1, v0, v1
	v_pack_b32_f16 v0, v2, v1
	v_fma_mixlo_f16 v2, v124, v31, 0
	v_alignbit_b32 v1, v2, v1, 16
	v_bitop3_b32 v2, v164, v120, 7 bitop3:0x36
	v_lshl_or_b32 v2, v2, 4, v121
	ds_write_b64 v2, v[0:1]
	v_lshl_add_u64 v[0:1], s[0:1], 0, v[172:173]
	v_lshlrev_b32_e32 v172, 2, v127
	v_lshl_add_u64 v[0:1], v[0:1], 0, v[172:173]
	s_waitcnt lgkmcnt(0)
	s_barrier
	global_load_dwordx4 v[108:111], v[0:1], off
	global_load_dwordx4 v[104:107], v[0:1], off offset:32
	global_load_dwordx4 v[100:103], v[0:1], off offset:64
	global_load_dwordx4 v[96:99], v[0:1], off offset:96
	v_xor_b32_e32 v0, v119, v120
	v_bitop3_b32 v8, v119, v120, 2 bitop3:0x36
	v_lshlrev_b32_e32 v172, 4, v0
	v_lshlrev_b32_e32 v174, 4, v8
	v_add_u32_e32 v0, v117, v172
	v_add_u32_e32 v8, v117, v174
	v_or_b32_e32 v1, 0x18000, v0
	v_add_u32_e32 v4, 0x1a000, v0
	v_or_b32_e32 v9, 0x18000, v8
	v_add_u32_e32 v8, 0x1a000, v8
	ds_read_b128 v[0:3], v1
	ds_read_b128 v[4:7], v4
	ds_read_b128 v[112:115], v9
	ds_read_b128 v[128:131], v8
	v_bitop3_b32 v8, v119, v120, 4 bitop3:0x36
	v_lshlrev_b32_e32 v175, 4, v8
	v_add_u32_e32 v8, v117, v175
	v_or_b32_e32 v9, 0x18000, v8
	v_add_u32_e32 v8, 0x1a000, v8
	ds_read_b128 v[132:135], v9
	ds_read_b128 v[136:139], v8
	v_bitop3_b32 v8, v119, v120, 6 bitop3:0x36
	v_lshlrev_b32_e32 v176, 4, v8
	v_add_u32_e32 v8, v117, v176
	v_or_b32_e32 v9, 0x18000, v8
	v_add_u32_e32 v8, 0x1a000, v8
	ds_read_b128 v[140:143], v9
	ds_read_b128 v[144:147], v8
	v_bitop3_b32 v8, v119, v120, 8 bitop3:0x36
	v_lshlrev_b32_e32 v177, 4, v8
	v_add_u32_e32 v8, v122, v177
	v_add_u32_e32 v9, v123, v177
	ds_read_b128 v[148:151], v8
	ds_read_b128 v[152:155], v9
	v_bitop3_b32 v8, v119, v120, 10 bitop3:0x36
	v_lshlrev_b32_e32 v178, 4, v8
	v_add_u32_e32 v8, v122, v178
	v_add_u32_e32 v9, v123, v178
	ds_read_b128 v[156:159], v8
	ds_read_b128 v[160:163], v9
	v_bitop3_b32 v8, v119, v120, 12 bitop3:0x36
	v_lshlrev_b32_e32 v179, 4, v8
	v_add_u32_e32 v8, v122, v179
	v_add_u32_e32 v9, v123, v179
	ds_read_b128 v[164:167], v8
	ds_read_b128 v[168:171], v9
	v_bitop3_b32 v8, v119, v120, 14 bitop3:0x36
	v_lshlrev_b32_e32 v180, 4, v8
	v_add_u32_e32 v8, v122, v180
	v_add_u32_e32 v9, v123, v180
	ds_read_b128 v[118:121], v8
	ds_read_b128 v[122:125], v9
	s_waitcnt vmcnt(19) lgkmcnt(14)
	v_mfma_f32_32x32x16_f16 v[16:31], v[36:39], v[0:3], 0
	v_mfma_f32_32x32x16_f16 v[0:15], v[36:39], v[4:7], 0
	s_waitcnt vmcnt(18) lgkmcnt(13)
	v_mfma_f32_32x32x16_f16 v[16:31], v[32:35], v[112:115], v[16:31]
	s_waitcnt lgkmcnt(12)
	v_mfma_f32_32x32x16_f16 v[0:15], v[32:35], v[128:131], v[0:15]
	s_waitcnt vmcnt(17) lgkmcnt(11)
	v_mfma_f32_32x32x16_f16 v[16:31], v[64:67], v[132:135], v[16:31]
	s_waitcnt lgkmcnt(10)
	v_mfma_f32_32x32x16_f16 v[0:15], v[64:67], v[136:139], v[0:15]
	s_waitcnt vmcnt(16) lgkmcnt(9)
	v_mfma_f32_32x32x16_f16 v[16:31], v[48:51], v[140:143], v[16:31]
	s_waitcnt lgkmcnt(8)
	v_mfma_f32_32x32x16_f16 v[0:15], v[48:51], v[144:147], v[0:15]
	v_or_b32_e32 v140, 0x1c000, v117
	v_or_b32_e32 v117, 0x1e000, v117
	v_add_u32_e32 v32, v140, v172
	v_add_u32_e32 v36, v117, v172
	v_add_u32_e32 v48, v140, v174
	v_add_u32_e32 v64, v117, v174
	v_add_u32_e32 v112, v140, v175
	v_add_u32_e32 v128, v117, v175
	v_add_u32_e32 v132, v140, v176
	v_add_u32_e32 v136, v117, v176
	ds_read_b128 v[32:35], v32
	ds_read_b128 v[36:39], v36
	ds_read_b128 v[48:51], v48
	ds_read_b128 v[64:67], v64
	ds_read_b128 v[112:115], v112
	ds_read_b128 v[128:131], v128
	ds_read_b128 v[132:135], v132
	ds_read_b128 v[136:139], v136
	s_waitcnt vmcnt(13) lgkmcnt(14)
	v_mfma_f32_32x32x16_f16 v[16:31], v[92:95], v[148:151], v[16:31]
	v_mfma_f32_32x32x16_f16 v[0:15], v[92:95], v[152:155], v[0:15]
	s_waitcnt lgkmcnt(13)
	v_mfma_f32_32x32x16_f16 v[16:31], v[84:87], v[156:159], v[16:31]
	s_waitcnt lgkmcnt(12)
	v_mfma_f32_32x32x16_f16 v[0:15], v[84:87], v[160:163], v[0:15]
	s_waitcnt lgkmcnt(11)
	v_mfma_f32_32x32x16_f16 v[16:31], v[80:83], v[164:167], v[16:31]
	s_waitcnt lgkmcnt(10)
	v_mfma_f32_32x32x16_f16 v[0:15], v[80:83], v[168:171], v[0:15]
	s_waitcnt vmcnt(8) lgkmcnt(9)
	v_mfma_f32_32x32x16_f16 v[16:31], v[88:91], v[118:121], v[16:31]
	s_waitcnt lgkmcnt(8)
	v_mfma_f32_32x32x16_f16 v[0:15], v[88:91], v[122:125], v[0:15]
	v_add_u32_e32 v80, v140, v177
	v_add_u32_e32 v84, v117, v177
	v_add_u32_e32 v88, v140, v178
	v_add_u32_e32 v92, v117, v178
	v_add_u32_e32 v118, v140, v179
	v_add_u32_e32 v122, v117, v179
	v_add_u32_e32 v140, v140, v180
	ds_read_b128 v[80:83], v80
	ds_read_b128 v[84:87], v84
	ds_read_b128 v[88:91], v88
	ds_read_b128 v[92:95], v92
	ds_read_b128 v[118:121], v118
	ds_read_b128 v[122:125], v122
	v_add_u32_e32 v117, v117, v180
	ds_read_b128 v[140:143], v140
	ds_read_b128 v[144:147], v117
	s_waitcnt lgkmcnt(14)
	v_mfma_f32_32x32x16_f16 v[16:31], v[76:79], v[32:35], v[16:31]
	v_mfma_f32_32x32x16_f16 v[0:15], v[76:79], v[36:39], v[0:15]
	s_waitcnt lgkmcnt(13)
	v_mfma_f32_32x32x16_f16 v[16:31], v[72:75], v[48:51], v[16:31]
	s_waitcnt lgkmcnt(12)
	v_mfma_f32_32x32x16_f16 v[0:15], v[72:75], v[64:67], v[0:15]
	s_waitcnt lgkmcnt(11)
	v_mfma_f32_32x32x16_f16 v[16:31], v[68:71], v[112:115], v[16:31]
	s_waitcnt lgkmcnt(10)
	v_mfma_f32_32x32x16_f16 v[0:15], v[68:71], v[128:131], v[0:15]
	s_waitcnt lgkmcnt(9)
	v_mfma_f32_32x32x16_f16 v[16:31], v[52:55], v[132:135], v[16:31]
	s_waitcnt lgkmcnt(8)
	v_mfma_f32_32x32x16_f16 v[0:15], v[52:55], v[136:139], v[0:15]
	s_waitcnt vmcnt(7) lgkmcnt(7)
	v_mfma_f32_32x32x16_f16 v[16:31], v[60:63], v[80:83], v[16:31]
	s_waitcnt lgkmcnt(6)
	v_mfma_f32_32x32x16_f16 v[0:15], v[60:63], v[84:87], v[0:15]
	s_waitcnt vmcnt(6) lgkmcnt(5)
	v_mfma_f32_32x32x16_f16 v[16:31], v[56:59], v[88:91], v[16:31]
	s_waitcnt lgkmcnt(4)
	v_mfma_f32_32x32x16_f16 v[0:15], v[56:59], v[92:95], v[0:15]
	s_waitcnt vmcnt(5) lgkmcnt(3)
	v_mfma_f32_32x32x16_f16 v[16:31], v[44:47], v[118:121], v[16:31]
	s_waitcnt lgkmcnt(2)
	v_mfma_f32_32x32x16_f16 v[0:15], v[44:47], v[122:125], v[0:15]
	s_waitcnt vmcnt(4) lgkmcnt(1)
	v_mfma_f32_32x32x16_f16 v[16:31], v[40:43], v[140:143], v[16:31]
	s_waitcnt lgkmcnt(0)
	v_mfma_f32_32x32x16_f16 v[0:15], v[40:43], v[144:147], v[0:15]
	s_lshl_b64 s[0:1], s[2:3], 22
	s_add_u32 s0, s12, s0
	v_or_b32_e32 v32, s14, v116
	s_addc_u32 s1, s13, s1
	v_lshlrev_b32_e32 v172, 3, v32
	v_or_b32_e32 v36, v126, v127
	v_lshl_add_u64 v[32:33], s[0:1], 0, v[172:173]
	v_lshlrev_b32_e32 v172, 14, v36
	v_lshl_add_u64 v[32:33], v[32:33], 0, v[172:173]
	s_nop 0
	v_mov_b32_e32 v34, v16
	s_nop 0
	v_mov_b32_e32 v35, v0
	v_mov_b32_e32 v0, v17
	v_add_co_u32_e32 v16, vcc, s5, v32
	s_waitcnt vmcnt(3)
	v_pk_add_f32 v[0:1], v[108:109], v[0:1] op_sel:[1,0]
	v_addc_co_u32_e32 v17, vcc, 0, v33, vcc
	s_mov_b32 s0, 0x8000
	global_store_dwordx2 v[16:17], v[0:1], off nt
	v_mov_b32_e32 v0, v18
	v_mov_b32_e32 v1, v2
	v_add_co_u32_e32 v16, vcc, s0, v32
	v_pk_add_f32 v[0:1], v[110:111], v[0:1] op_sel_hi:[0,1]
	s_nop 0
	v_addc_co_u32_e32 v17, vcc, 0, v33, vcc
	global_store_dwordx2 v[16:17], v[0:1], off nt
	v_mov_b32_e32 v0, v111
	v_mov_b32_e32 v2, v19
	v_pk_add_f32 v[0:1], v[0:1], v[2:3] op_sel_hi:[0,1]
	v_add_co_u32_e32 v2, vcc, s4, v32
	s_mov_b32 s0, 0x24000
	s_nop 0
	v_addc_co_u32_e32 v3, vcc, 0, v33, vcc
	global_store_dwordx2 v[2:3], v[0:1], off nt
	v_mov_b32_e32 v0, v20
	v_mov_b32_e32 v1, v4
	v_add_co_u32_e32 v2, vcc, s6, v32
	s_waitcnt vmcnt(5)
	v_pk_add_f32 v[0:1], v[104:105], v[0:1] op_sel_hi:[0,1]
	v_addc_co_u32_e32 v3, vcc, 0, v33, vcc
	global_store_dwordx2 v[2:3], v[0:1], off nt
	v_mov_b32_e32 v4, v21
	v_add_co_u32_e32 v2, vcc, s0, v32
	v_pk_add_f32 v[0:1], v[104:105], v[4:5] op_sel:[1,0]
	s_nop 0
	v_addc_co_u32_e32 v3, vcc, 0, v33, vcc
	s_mov_b32 s0, 0x28000
	global_store_dwordx2 v[2:3], v[0:1], off nt
	v_mov_b32_e32 v0, v22
	v_mov_b32_e32 v1, v6
	v_add_co_u32_e32 v2, vcc, s0, v32
	v_pk_add_f32 v[0:1], v[106:107], v[0:1] op_sel_hi:[0,1]
	s_nop 0
	v_addc_co_u32_e32 v3, vcc, 0, v33, vcc
	s_mov_b32 s0, 0x2c000
	global_store_dwordx2 v[2:3], v[0:1], off nt
	v_mov_b32_e32 v0, v107
	v_mov_b32_e32 v6, v23
	v_add_co_u32_e32 v2, vcc, s0, v32
	v_pk_add_f32 v[0:1], v[0:1], v[6:7] op_sel_hi:[0,1]
	s_nop 0
	v_addc_co_u32_e32 v3, vcc, 0, v33, vcc
	s_mov_b32 s0, 0x40000
	global_store_dwordx2 v[2:3], v[0:1], off nt
	v_mov_b32_e32 v0, v24
	v_mov_b32_e32 v1, v8
	v_add_co_u32_e32 v2, vcc, s0, v32
	s_waitcnt vmcnt(8)
	v_pk_add_f32 v[0:1], v[100:101], v[0:1] op_sel_hi:[0,1]
	v_addc_co_u32_e32 v3, vcc, 0, v33, vcc
	s_mov_b32 s0, 0x44000
	global_store_dwordx2 v[2:3], v[0:1], off nt
	v_mov_b32_e32 v8, v25
	v_add_co_u32_e32 v2, vcc, s0, v32
	v_pk_add_f32 v[0:1], v[100:101], v[8:9] op_sel:[1,0]
	s_nop 0
	v_addc_co_u32_e32 v3, vcc, 0, v33, vcc
	s_mov_b32 s0, 0x48000
	global_store_dwordx2 v[2:3], v[0:1], off nt
	v_mov_b32_e32 v0, v26
	v_mov_b32_e32 v1, v10
	v_add_co_u32_e32 v2, vcc, s0, v32
	v_pk_add_f32 v[0:1], v[102:103], v[0:1] op_sel_hi:[0,1]
	s_nop 0
	v_addc_co_u32_e32 v3, vcc, 0, v33, vcc
	s_mov_b32 s0, 0x4c000
	global_store_dwordx2 v[2:3], v[0:1], off nt
	v_mov_b32_e32 v0, v103
	v_mov_b32_e32 v10, v27
	v_add_co_u32_e32 v2, vcc, s0, v32
	v_pk_add_f32 v[0:1], v[0:1], v[10:11] op_sel_hi:[0,1]
	s_nop 0
	v_addc_co_u32_e32 v3, vcc, 0, v33, vcc
	s_mov_b32 s0, 0x60000
	global_store_dwordx2 v[2:3], v[0:1], off nt
	v_mov_b32_e32 v0, v28
	v_mov_b32_e32 v1, v12
	v_add_co_u32_e32 v2, vcc, s0, v32
	s_waitcnt vmcnt(11)
	v_pk_add_f32 v[0:1], v[96:97], v[0:1] op_sel_hi:[0,1]
	v_addc_co_u32_e32 v3, vcc, 0, v33, vcc
	s_mov_b32 s0, 0x64000
	global_store_dwordx2 v[2:3], v[0:1], off nt
	v_mov_b32_e32 v12, v29
	v_add_co_u32_e32 v2, vcc, s0, v32
	v_pk_add_f32 v[0:1], v[96:97], v[12:13] op_sel:[1,0]
	s_nop 0
	v_addc_co_u32_e32 v3, vcc, 0, v33, vcc
	s_mov_b32 s0, 0x68000
	global_store_dwordx2 v[2:3], v[0:1], off nt
	v_mov_b32_e32 v0, v30
	v_mov_b32_e32 v1, v14
	v_add_co_u32_e32 v2, vcc, s0, v32
	v_pk_add_f32 v[0:1], v[98:99], v[0:1] op_sel_hi:[0,1]
	s_nop 0
	v_addc_co_u32_e32 v3, vcc, 0, v33, vcc
	global_store_dwordx2 v[2:3], v[0:1], off nt
	v_mov_b32_e32 v0, v99
	v_mov_b32_e32 v14, v31
	v_add_co_u32_e32 v2, vcc, 0x6c000, v32
	v_pk_add_f32 v[34:35], v[108:109], v[34:35] op_sel_hi:[0,1]
	v_pk_add_f32 v[0:1], v[0:1], v[14:15] op_sel_hi:[0,1]
	v_addc_co_u32_e32 v3, vcc, 0, v33, vcc
	global_store_dwordx2 v[32:33], v[34:35], off nt
	global_store_dwordx2 v[2:3], v[0:1], off nt
	s_endpgm

	.amdhsa_kernel _Z7na_mainPKDF16_PKhS0_PKfS4_S4_S4_Pf
		.amdhsa_group_segment_fixed_size 162048
		.amdhsa_private_segment_fixed_size 0
		.amdhsa_kernarg_size 64
		.amdhsa_user_sgpr_count 2
		.amdhsa_user_sgpr_dispatch_ptr 0
		.amdhsa_user_sgpr_queue_ptr 0
		.amdhsa_user_sgpr_kernarg_segment_ptr 1
		.amdhsa_user_sgpr_dispatch_id 0
		.amdhsa_user_sgpr_kernarg_preload_length 0
		.amdhsa_user_sgpr_kernarg_preload_offset 0
		.amdhsa_user_sgpr_private_segment_size 0
		.amdhsa_uses_dynamic_stack 0
		.amdhsa_enable_private_segment 0
		.amdhsa_system_sgpr_workgroup_id_x 1
		.amdhsa_system_sgpr_workgroup_id_y 0
		.amdhsa_system_sgpr_workgroup_id_z 0
		.amdhsa_system_sgpr_workgroup_info 0
		.amdhsa_system_vgpr_workitem_id 0
		.amdhsa_next_free_vgpr 236
		.amdhsa_next_free_sgpr 96
		.amdhsa_accum_offset 236
		.amdhsa_reserve_vcc 1
		.amdhsa_float_round_mode_32 0
		.amdhsa_float_round_mode_16_64 0
		.amdhsa_float_denorm_mode_32 3
		.amdhsa_float_denorm_mode_16_64 3
		.amdhsa_dx10_clamp 1
		.amdhsa_ieee_mode 1
		.amdhsa_fp16_overflow 0
		.amdhsa_tg_split 0
		.amdhsa_exception_fp_ieee_invalid_op 0
		.amdhsa_exception_fp_denorm_src 0
		.amdhsa_exception_fp_ieee_div_zero 0
		.amdhsa_exception_fp_ieee_overflow 0
		.amdhsa_exception_fp_ieee_underflow 0
		.amdhsa_exception_fp_ieee_inexact 0
		.amdhsa_exception_int_div_zero 0
	.end_amdhsa_kernel

amdhsa.kernels:
  - .agpr_count:     16
    .args:
      - .actual_access:  read_only
        .address_space:  global
        .offset:         0
        .size:           8
        .value_kind:     global_buffer
      - .actual_access:  read_only
        .address_space:  global
        .offset:         8
        .size:           8
        .value_kind:     global_buffer
      - .actual_access:  read_only
        .address_space:  global
        .offset:         16
        .size:           8
        .value_kind:     global_buffer
      - .actual_access:  read_only
        .address_space:  global
        .offset:         24
        .size:           8
        .value_kind:     global_buffer
      - .actual_access:  read_only
        .address_space:  global
        .offset:         32
        .size:           8
        .value_kind:     global_buffer
      - .actual_access:  read_only
        .address_space:  global
        .offset:         40
        .size:           8
        .value_kind:     global_buffer
      - .actual_access:  write_only
        .address_space:  global
        .offset:         48
        .size:           8
        .value_kind:     global_buffer
      - .actual_access:  write_only
        .address_space:  global
        .offset:         56
        .size:           8
        .value_kind:     global_buffer
      - .actual_access:  write_only
        .address_space:  global
        .offset:         64
        .size:           8
        .value_kind:     global_buffer
      - .actual_access:  write_only
        .address_space:  global
        .offset:         72
        .size:           8
        .value_kind:     global_buffer
      - .actual_access:  write_only
        .address_space:  global
        .offset:         80
        .size:           8
        .value_kind:     global_buffer
      - .actual_access:  write_only
        .address_space:  global
        .offset:         88
        .size:           8
        .value_kind:     global_buffer
    .group_segment_fixed_size: 50176
    .kernarg_segment_align: 8
    .kernarg_segment_size: 96
    .language:       OpenCL C
    .language_version:
      - 2
      - 0
    .max_flat_workgroup_size: 256
    .name:           _Z7na_prepPKfS0_S0_S0_S0_S0_PDF16_PhS1_PfS3_S3_
    .private_segment_fixed_size: 0
    .sgpr_count:     23
    .sgpr_spill_count: 0
    .symbol:         _Z7na_prepPKfS0_S0_S0_S0_S0_PDF16_PhS1_PfS3_S3_.kd
    .uniform_work_group_size: 1
    .uses_dynamic_stack: false
    .vgpr_count:     116
    .vgpr_spill_count: 0
    .wavefront_size: 64
  - .agpr_count:     0
    .args:
      - .address_space:  global
        .offset:         0
        .size:           8
        .value_kind:     global_buffer
      - .actual_access:  read_only
        .address_space:  global
        .offset:         8
        .size:           8
        .value_kind:     global_buffer
      - .actual_access:  read_only
        .address_space:  global
        .offset:         16
        .size:           8
        .value_kind:     global_buffer
      - .actual_access:  read_only
        .address_space:  global
        .offset:         24
        .size:           8
        .value_kind:     global_buffer
      - .actual_access:  read_only
        .address_space:  global
        .offset:         32
        .size:           8
        .value_kind:     global_buffer
      - .actual_access:  read_only
        .address_space:  global
        .offset:         40
        .size:           8
        .value_kind:     global_buffer
      - .actual_access:  read_only
        .address_space:  global
        .offset:         48
        .size:           8
        .value_kind:     global_buffer
      - .actual_access:  write_only
        .address_space:  global
        .offset:         56
        .size:           8
        .value_kind:     global_buffer
    .group_segment_fixed_size: 162048
    .kernarg_segment_align: 8
    .kernarg_segment_size: 64
    .language:       OpenCL C
    .language_version:
      - 2
      - 0
    .max_flat_workgroup_size: 512
    .name:           _Z7na_mainPKDF16_PKhS0_PKfS4_S4_S4_Pf
    .private_segment_fixed_size: 0
    .sgpr_count:     24
    .sgpr_spill_count: 0
    .symbol:         _Z7na_mainPKDF16_PKhS0_PKfS4_S4_S4_Pf.kd
    .uniform_work_group_size: 1
    .uses_dynamic_stack: false
    .vgpr_count:     236
    .vgpr_spill_count: 0
    .wavefront_size: 64
